# plan P: in-proj-0 with 29 conversion WGs (7 GEMM rounds on 227 WGs); the displaced gate/up experts converted by all waves at the start of norm1
# baseline (speedup 1.0000x reference)
.LBB0_184:
	s_load_dwordx4 s[0:3], s[8:9], 0x138
	s_waitcnt lgkmcnt(0)
	s_mov_b64 s[4:5], s[0:1]
	s_cmp_lt_i32 s4, 2
	s_cselect_b64 s[0:1], -1, 0
	s_cmp_gt_i32 s5, 1
	s_cselect_b64 s[2:3], -1, 0
	s_and_b64 s[0:1], s[0:1], s[2:3]
	s_andn2_b64 vcc, exec, s[0:1]
	s_cbranch_vccnz .LBB0_254
	v_readlane_b32 s4, v243, 0
	s_lshl_b32 s4, s4, 3
	s_add_i32 s19, s4, s94
	s_mov_b32 s4, s19
	s_mov_b32 s5, 0x800
	s_mov_b32 s6, 0x1400
	s_waitcnt vmcnt(0)
	s_cmp_ge_u32 s4, s6
	s_cbranch_scc1 .Lp1c0_done
	v_readlane_b32 s8, v243, 7
	v_readlane_b32 s9, v243, 8
	s_load_dwordx2 s[10:11], s[8:9], 0x130
	s_load_dwordx2 s[12:13], s[8:9], 0xf8
	s_load_dwordx2 s[14:15], s[8:9], 0x108
	v_mbcnt_lo_u32_b32 v150, -1, 0
	v_mbcnt_hi_u32_b32 v150, -1, v150
	v_lshrrev_b32_e32 v151, 3, v150
	v_and_b32_e32 v150, 7, v150
	v_lshlrev_b32_e32 v144, 16, v151
	v_lshl_add_u32 v144, v150, 4, v144
	v_add_u32_e32 v145, 0x1000, v144
	v_add_u32_e32 v146, 0x2000, v144
	v_add_u32_e32 v147, 0x3000, v144
	v_lshlrev_b32_e32 v148, 12, v150
	v_lshl_add_u32 v148, v151, 4, v148
	v_mov_b32_e32 v149, 0x43e00000
	s_mov_b32 s28, 0xc3e00000
	s_waitcnt lgkmcnt(0)
	s_add_u32 s10, s10, 0x2900000
	s_addc_u32 s11, s11, 0
	s_lshr_b32 s22, s4, 8
	s_and_b32 s23, s4, 0xff
	s_and_b32 s27, s22, 1
	s_lshr_b32 s22, s22, 1
	s_cmp_eq_u32 s27, 0
	s_cselect_b64 s[16:17], s[12:13], s[14:15]
	s_add_i32 s22, s22, 37
	s_lshl_b32 s24, s22, 22
	s_lshr_b32 s25, s23, 5
	s_lshl_b32 s25, s25, 19
	s_and_b32 s26, s23, 31
	s_lshl_b32 s26, s26, 7
	s_add_i32 s24, s24, s25
	s_add_i32 s24, s24, s26
	s_add_u32 s16, s16, s24
	s_addc_u32 s17, s17, 0
	s_nop 0
	global_load_dwordx4 v[0:3], v144, s[16:17] nt
	global_load_dwordx4 v[4:7], v145, s[16:17] nt
	global_load_dwordx4 v[8:11], v146, s[16:17] nt
	global_load_dwordx4 v[12:15], v147, s[16:17] nt
	s_add_u32 s16, s16, 0x4000
	s_addc_u32 s17, s17, 0
	s_nop 0
	global_load_dwordx4 v[16:19], v144, s[16:17] nt
	global_load_dwordx4 v[20:23], v145, s[16:17] nt
	global_load_dwordx4 v[24:27], v146, s[16:17] nt
	global_load_dwordx4 v[28:31], v147, s[16:17] nt
	s_add_u32 s16, s16, 0x4000
	s_addc_u32 s17, s17, 0
	s_nop 0
	global_load_dwordx4 v[32:35], v144, s[16:17] nt
	global_load_dwordx4 v[36:39], v145, s[16:17] nt
	global_load_dwordx4 v[40:43], v146, s[16:17] nt
	global_load_dwordx4 v[44:47], v147, s[16:17] nt
	s_add_u32 s16, s16, 0x4000
	s_addc_u32 s17, s17, 0
	s_nop 0
	global_load_dwordx4 v[48:51], v144, s[16:17] nt
	global_load_dwordx4 v[52:55], v145, s[16:17] nt
	global_load_dwordx4 v[56:59], v146, s[16:17] nt
	global_load_dwordx4 v[60:63], v147, s[16:17] nt
	s_add_i32 s7, s4, s5
	s_cmp_lt_u32 s7, s6
	s_cbranch_scc0 .Lp1c0_p_last
	s_lshr_b32 s22, s7, 8
	s_and_b32 s23, s7, 0xff
	s_and_b32 s27, s22, 1
	s_lshr_b32 s22, s22, 1
	s_cmp_eq_u32 s27, 0
	s_cselect_b64 s[16:17], s[12:13], s[14:15]
	s_add_i32 s22, s22, 37
	s_lshl_b32 s24, s22, 22
	s_lshr_b32 s25, s23, 5
	s_lshl_b32 s25, s25, 19
	s_and_b32 s26, s23, 31
	s_lshl_b32 s26, s26, 7
	s_add_i32 s24, s24, s25
	s_add_i32 s24, s24, s26
	s_add_u32 s16, s16, s24
	s_addc_u32 s17, s17, 0
	s_nop 0
	global_load_dwordx4 v[64:67], v144, s[16:17] nt
	global_load_dwordx4 v[68:71], v145, s[16:17] nt
	global_load_dwordx4 v[72:75], v146, s[16:17] nt
	global_load_dwordx4 v[76:79], v147, s[16:17] nt
	s_add_u32 s16, s16, 0x4000
	s_addc_u32 s17, s17, 0
	s_nop 0
	global_load_dwordx4 v[80:83], v144, s[16:17] nt
	global_load_dwordx4 v[84:87], v145, s[16:17] nt
	global_load_dwordx4 v[88:91], v146, s[16:17] nt
	global_load_dwordx4 v[92:95], v147, s[16:17] nt
	s_add_u32 s16, s16, 0x4000
	s_addc_u32 s17, s17, 0
	s_nop 0
	global_load_dwordx4 v[96:99], v144, s[16:17] nt
	global_load_dwordx4 v[100:103], v145, s[16:17] nt
	global_load_dwordx4 v[104:107], v146, s[16:17] nt
	global_load_dwordx4 v[108:111], v147, s[16:17] nt
	s_add_u32 s16, s16, 0x4000
	s_addc_u32 s17, s17, 0
	s_nop 0
	global_load_dwordx4 v[112:115], v144, s[16:17] nt
	global_load_dwordx4 v[116:119], v145, s[16:17] nt
	global_load_dwordx4 v[120:123], v146, s[16:17] nt
	global_load_dwordx4 v[124:127], v147, s[16:17] nt
	s_waitcnt vmcnt(16)
	s_branch .Lp1c0_p_st

.Lp1c0_p_st:
	s_lshr_b32 s22, s4, 8
	s_and_b32 s23, s4, 0xff
	s_and_b32 s27, s22, 1
	s_lshr_b32 s22, s22, 1
	s_add_i32 s22, s22, 37
	s_mul_i32 s24, s22, 0x300000
	s_lshr_b32 s25, s23, 5
	s_lshl_b32 s25, s25, 7
	s_add_i32 s24, s24, s25
	s_and_b32 s26, s23, 31
	s_lshr_b32 s25, s26, 2
	s_lshl_b32 s25, s25, 18
	s_add_i32 s24, s24, s25
	s_lshl_b32 s25, s27, 17
	s_add_i32 s24, s24, s25
	s_and_b32 s25, s26, 3
	s_lshl_b32 s25, s25, 15
	s_add_i32 s24, s24, s25
	s_add_u32 s20, s10, s24
	s_addc_u32 s21, s11, 0
	v_mul_f32_e32 v0, 0x42000000, v0
	v_mul_f32_e32 v4, 0x42000000, v4
	v_mul_f32_e32 v8, 0x42000000, v8
	v_mul_f32_e32 v12, 0x42000000, v12
	v_mul_f32_e32 v16, 0x42000000, v16
	v_mul_f32_e32 v20, 0x42000000, v20
	v_mul_f32_e32 v24, 0x42000000, v24
	v_mul_f32_e32 v28, 0x42000000, v28
	v_mul_f32_e32 v32, 0x42000000, v32
	v_mul_f32_e32 v36, 0x42000000, v36
	v_mul_f32_e32 v40, 0x42000000, v40
	v_mul_f32_e32 v44, 0x42000000, v44
	v_mul_f32_e32 v48, 0x42000000, v48
	v_mul_f32_e32 v52, 0x42000000, v52
	v_mul_f32_e32 v56, 0x42000000, v56
	v_mul_f32_e32 v60, 0x42000000, v60
	v_med3_f32 v0, v0, s28, v149
	v_med3_f32 v4, v4, s28, v149
	v_med3_f32 v8, v8, s28, v149
	v_med3_f32 v12, v12, s28, v149
	v_med3_f32 v16, v16, s28, v149
	v_med3_f32 v20, v20, s28, v149
	v_med3_f32 v24, v24, s28, v149
	v_med3_f32 v28, v28, s28, v149
	v_med3_f32 v32, v32, s28, v149
	v_med3_f32 v36, v36, s28, v149
	v_med3_f32 v40, v40, s28, v149
	v_med3_f32 v44, v44, s28, v149
	v_med3_f32 v48, v48, s28, v149
	v_med3_f32 v52, v52, s28, v149
	v_med3_f32 v56, v56, s28, v149
	v_med3_f32 v60, v60, s28, v149
	v_cvt_pk_fp8_f32 v136, v0, v4
	v_cvt_pk_fp8_f32 v137, v16, v20
	v_cvt_pk_fp8_f32 v138, v32, v36
	v_cvt_pk_fp8_f32 v139, v48, v52
	v_cvt_pk_fp8_f32 v136, v8, v12 op_sel:[0,0,1]
	v_cvt_pk_fp8_f32 v137, v24, v28 op_sel:[0,0,1]
	v_cvt_pk_fp8_f32 v138, v40, v44 op_sel:[0,0,1]
	v_cvt_pk_fp8_f32 v139, v56, v60 op_sel:[0,0,1]
	s_nop 0
	global_store_dwordx4 v148, v[136:139], s[20:21]
	v_mul_f32_e32 v1, 0x42000000, v1
	v_mul_f32_e32 v5, 0x42000000, v5
	v_mul_f32_e32 v9, 0x42000000, v9
	v_mul_f32_e32 v13, 0x42000000, v13
	v_mul_f32_e32 v17, 0x42000000, v17
	v_mul_f32_e32 v21, 0x42000000, v21
	v_mul_f32_e32 v25, 0x42000000, v25
	v_mul_f32_e32 v29, 0x42000000, v29
	v_mul_f32_e32 v33, 0x42000000, v33
	v_mul_f32_e32 v37, 0x42000000, v37
	v_mul_f32_e32 v41, 0x42000000, v41
	v_mul_f32_e32 v45, 0x42000000, v45
	v_mul_f32_e32 v49, 0x42000000, v49
	v_mul_f32_e32 v53, 0x42000000, v53
	v_mul_f32_e32 v57, 0x42000000, v57
	v_mul_f32_e32 v61, 0x42000000, v61
	v_med3_f32 v1, v1, s28, v149
	v_med3_f32 v5, v5, s28, v149
	v_med3_f32 v9, v9, s28, v149
	v_med3_f32 v13, v13, s28, v149
	v_med3_f32 v17, v17, s28, v149
	v_med3_f32 v21, v21, s28, v149
	v_med3_f32 v25, v25, s28, v149
	v_med3_f32 v29, v29, s28, v149
	v_med3_f32 v33, v33, s28, v149
	v_med3_f32 v37, v37, s28, v149
	v_med3_f32 v41, v41, s28, v149
	v_med3_f32 v45, v45, s28, v149
	v_med3_f32 v49, v49, s28, v149
	v_med3_f32 v53, v53, s28, v149
	v_med3_f32 v57, v57, s28, v149
	v_med3_f32 v61, v61, s28, v149
	v_cvt_pk_fp8_f32 v140, v1, v5
	v_cvt_pk_fp8_f32 v141, v17, v21
	v_cvt_pk_fp8_f32 v142, v33, v37
	v_cvt_pk_fp8_f32 v143, v49, v53
	v_cvt_pk_fp8_f32 v140, v9, v13 op_sel:[0,0,1]
	v_cvt_pk_fp8_f32 v141, v25, v29 op_sel:[0,0,1]
	v_cvt_pk_fp8_f32 v142, v41, v45 op_sel:[0,0,1]
	v_cvt_pk_fp8_f32 v143, v57, v61 op_sel:[0,0,1]
	s_nop 0
	global_store_dwordx4 v148, v[140:143], s[20:21] offset:1024
	v_mul_f32_e32 v2, 0x42000000, v2
	v_mul_f32_e32 v6, 0x42000000, v6
	v_mul_f32_e32 v10, 0x42000000, v10
	v_mul_f32_e32 v14, 0x42000000, v14
	v_mul_f32_e32 v18, 0x42000000, v18
	v_mul_f32_e32 v22, 0x42000000, v22
	v_mul_f32_e32 v26, 0x42000000, v26
	v_mul_f32_e32 v30, 0x42000000, v30
	v_mul_f32_e32 v34, 0x42000000, v34
	v_mul_f32_e32 v38, 0x42000000, v38
	v_mul_f32_e32 v42, 0x42000000, v42
	v_mul_f32_e32 v46, 0x42000000, v46
	v_mul_f32_e32 v50, 0x42000000, v50
	v_mul_f32_e32 v54, 0x42000000, v54
	v_mul_f32_e32 v58, 0x42000000, v58
	v_mul_f32_e32 v62, 0x42000000, v62
	v_med3_f32 v2, v2, s28, v149
	v_med3_f32 v6, v6, s28, v149
	v_med3_f32 v10, v10, s28, v149
	v_med3_f32 v14, v14, s28, v149
	v_med3_f32 v18, v18, s28, v149
	v_med3_f32 v22, v22, s28, v149
	v_med3_f32 v26, v26, s28, v149
	v_med3_f32 v30, v30, s28, v149
	v_med3_f32 v34, v34, s28, v149
	v_med3_f32 v38, v38, s28, v149
	v_med3_f32 v42, v42, s28, v149
	v_med3_f32 v46, v46, s28, v149
	v_med3_f32 v50, v50, s28, v149
	v_med3_f32 v54, v54, s28, v149
	v_med3_f32 v58, v58, s28, v149
	v_med3_f32 v62, v62, s28, v149
	v_cvt_pk_fp8_f32 v136, v2, v6
	v_cvt_pk_fp8_f32 v137, v18, v22
	v_cvt_pk_fp8_f32 v138, v34, v38
	v_cvt_pk_fp8_f32 v139, v50, v54
	v_cvt_pk_fp8_f32 v136, v10, v14 op_sel:[0,0,1]
	v_cvt_pk_fp8_f32 v137, v26, v30 op_sel:[0,0,1]
	v_cvt_pk_fp8_f32 v138, v42, v46 op_sel:[0,0,1]
	v_cvt_pk_fp8_f32 v139, v58, v62 op_sel:[0,0,1]
	s_nop 0
	global_store_dwordx4 v148, v[136:139], s[20:21] offset:2048
	v_mul_f32_e32 v3, 0x42000000, v3
	v_mul_f32_e32 v7, 0x42000000, v7
	v_mul_f32_e32 v11, 0x42000000, v11
	v_mul_f32_e32 v15, 0x42000000, v15
	v_mul_f32_e32 v19, 0x42000000, v19
	v_mul_f32_e32 v23, 0x42000000, v23
	v_mul_f32_e32 v27, 0x42000000, v27
	v_mul_f32_e32 v31, 0x42000000, v31
	v_mul_f32_e32 v35, 0x42000000, v35
	v_mul_f32_e32 v39, 0x42000000, v39
	v_mul_f32_e32 v43, 0x42000000, v43
	v_mul_f32_e32 v47, 0x42000000, v47
	v_mul_f32_e32 v51, 0x42000000, v51
	v_mul_f32_e32 v55, 0x42000000, v55
	v_mul_f32_e32 v59, 0x42000000, v59
	v_mul_f32_e32 v63, 0x42000000, v63
	v_med3_f32 v3, v3, s28, v149
	v_med3_f32 v7, v7, s28, v149
	v_med3_f32 v11, v11, s28, v149
	v_med3_f32 v15, v15, s28, v149
	v_med3_f32 v19, v19, s28, v149
	v_med3_f32 v23, v23, s28, v149
	v_med3_f32 v27, v27, s28, v149
	v_med3_f32 v31, v31, s28, v149
	v_med3_f32 v35, v35, s28, v149
	v_med3_f32 v39, v39, s28, v149
	v_med3_f32 v43, v43, s28, v149
	v_med3_f32 v47, v47, s28, v149
	v_med3_f32 v51, v51, s28, v149
	v_med3_f32 v55, v55, s28, v149
	v_med3_f32 v59, v59, s28, v149
	v_med3_f32 v63, v63, s28, v149
	v_cvt_pk_fp8_f32 v140, v3, v7
	v_cvt_pk_fp8_f32 v141, v19, v23
	v_cvt_pk_fp8_f32 v142, v35, v39
	v_cvt_pk_fp8_f32 v143, v51, v55
	v_cvt_pk_fp8_f32 v140, v11, v15 op_sel:[0,0,1]
	v_cvt_pk_fp8_f32 v141, v27, v31 op_sel:[0,0,1]
	v_cvt_pk_fp8_f32 v142, v43, v47 op_sel:[0,0,1]
	v_cvt_pk_fp8_f32 v143, v59, v63 op_sel:[0,0,1]
	s_nop 0
	global_store_dwordx4 v148, v[140:143], s[20:21] offset:3072
	s_cmp_ge_u32 s7, s6
	s_cbranch_scc1 .Lp1c0_done
	s_mov_b32 s4, s7
.Lp1c0_loop:
	s_add_i32 s7, s4, s5
	s_cmp_lt_u32 s7, s6
	s_cbranch_scc0 .Lp1c0_B_last
	s_lshr_b32 s22, s7, 8
	s_and_b32 s23, s7, 0xff
	s_and_b32 s27, s22, 1
	s_lshr_b32 s22, s22, 1
	s_cmp_eq_u32 s27, 0
	s_cselect_b64 s[16:17], s[12:13], s[14:15]
	s_add_i32 s22, s22, 37
	s_lshl_b32 s24, s22, 22
	s_lshr_b32 s25, s23, 5
	s_lshl_b32 s25, s25, 19
	s_and_b32 s26, s23, 31
	s_lshl_b32 s26, s26, 7
	s_add_i32 s24, s24, s25
	s_add_i32 s24, s24, s26
	s_add_u32 s16, s16, s24
	s_addc_u32 s17, s17, 0
	s_nop 0
	global_load_dwordx4 v[0:3], v144, s[16:17] nt
	global_load_dwordx4 v[4:7], v145, s[16:17] nt
	global_load_dwordx4 v[8:11], v146, s[16:17] nt
	global_load_dwordx4 v[12:15], v147, s[16:17] nt
	s_add_u32 s16, s16, 0x4000
	s_addc_u32 s17, s17, 0
	s_nop 0
	global_load_dwordx4 v[16:19], v144, s[16:17] nt
	global_load_dwordx4 v[20:23], v145, s[16:17] nt
	global_load_dwordx4 v[24:27], v146, s[16:17] nt
	global_load_dwordx4 v[28:31], v147, s[16:17] nt
	s_add_u32 s16, s16, 0x4000
	s_addc_u32 s17, s17, 0
	s_nop 0
	global_load_dwordx4 v[32:35], v144, s[16:17] nt
	global_load_dwordx4 v[36:39], v145, s[16:17] nt
	global_load_dwordx4 v[40:43], v146, s[16:17] nt
	global_load_dwordx4 v[44:47], v147, s[16:17] nt
	s_add_u32 s16, s16, 0x4000
	s_addc_u32 s17, s17, 0
	s_nop 0
	global_load_dwordx4 v[48:51], v144, s[16:17] nt
	global_load_dwordx4 v[52:55], v145, s[16:17] nt
	global_load_dwordx4 v[56:59], v146, s[16:17] nt
	global_load_dwordx4 v[60:63], v147, s[16:17] nt
	s_waitcnt vmcnt(20)
	s_branch .Lp1c0_B_st

.Lp1c0_B_st:
	s_lshr_b32 s22, s4, 8
	s_and_b32 s23, s4, 0xff
	s_and_b32 s27, s22, 1
	s_lshr_b32 s22, s22, 1
	s_add_i32 s22, s22, 37
	s_mul_i32 s24, s22, 0x300000
	s_lshr_b32 s25, s23, 5
	s_lshl_b32 s25, s25, 7
	s_add_i32 s24, s24, s25
	s_and_b32 s26, s23, 31
	s_lshr_b32 s25, s26, 2
	s_lshl_b32 s25, s25, 18
	s_add_i32 s24, s24, s25
	s_lshl_b32 s25, s27, 17
	s_add_i32 s24, s24, s25
	s_and_b32 s25, s26, 3
	s_lshl_b32 s25, s25, 15
	s_add_i32 s24, s24, s25
	s_add_u32 s20, s10, s24
	s_addc_u32 s21, s11, 0
	v_mul_f32_e32 v64, 0x42000000, v64
	v_mul_f32_e32 v68, 0x42000000, v68
	v_mul_f32_e32 v72, 0x42000000, v72
	v_mul_f32_e32 v76, 0x42000000, v76
	v_mul_f32_e32 v80, 0x42000000, v80
	v_mul_f32_e32 v84, 0x42000000, v84
	v_mul_f32_e32 v88, 0x42000000, v88
	v_mul_f32_e32 v92, 0x42000000, v92
	v_mul_f32_e32 v96, 0x42000000, v96
	v_mul_f32_e32 v100, 0x42000000, v100
	v_mul_f32_e32 v104, 0x42000000, v104
	v_mul_f32_e32 v108, 0x42000000, v108
	v_mul_f32_e32 v112, 0x42000000, v112
	v_mul_f32_e32 v116, 0x42000000, v116
	v_mul_f32_e32 v120, 0x42000000, v120
	v_mul_f32_e32 v124, 0x42000000, v124
	v_med3_f32 v64, v64, s28, v149
	v_med3_f32 v68, v68, s28, v149
	v_med3_f32 v72, v72, s28, v149
	v_med3_f32 v76, v76, s28, v149
	v_med3_f32 v80, v80, s28, v149
	v_med3_f32 v84, v84, s28, v149
	v_med3_f32 v88, v88, s28, v149
	v_med3_f32 v92, v92, s28, v149
	v_med3_f32 v96, v96, s28, v149
	v_med3_f32 v100, v100, s28, v149
	v_med3_f32 v104, v104, s28, v149
	v_med3_f32 v108, v108, s28, v149
	v_med3_f32 v112, v112, s28, v149
	v_med3_f32 v116, v116, s28, v149
	v_med3_f32 v120, v120, s28, v149
	v_med3_f32 v124, v124, s28, v149
	v_cvt_pk_fp8_f32 v136, v64, v68
	v_cvt_pk_fp8_f32 v137, v80, v84
	v_cvt_pk_fp8_f32 v138, v96, v100
	v_cvt_pk_fp8_f32 v139, v112, v116
	v_cvt_pk_fp8_f32 v136, v72, v76 op_sel:[0,0,1]
	v_cvt_pk_fp8_f32 v137, v88, v92 op_sel:[0,0,1]
	v_cvt_pk_fp8_f32 v138, v104, v108 op_sel:[0,0,1]
	v_cvt_pk_fp8_f32 v139, v120, v124 op_sel:[0,0,1]
	s_nop 0
	global_store_dwordx4 v148, v[136:139], s[20:21]
	v_mul_f32_e32 v65, 0x42000000, v65
	v_mul_f32_e32 v69, 0x42000000, v69
	v_mul_f32_e32 v73, 0x42000000, v73
	v_mul_f32_e32 v77, 0x42000000, v77
	v_mul_f32_e32 v81, 0x42000000, v81
	v_mul_f32_e32 v85, 0x42000000, v85
	v_mul_f32_e32 v89, 0x42000000, v89
	v_mul_f32_e32 v93, 0x42000000, v93
	v_mul_f32_e32 v97, 0x42000000, v97
	v_mul_f32_e32 v101, 0x42000000, v101
	v_mul_f32_e32 v105, 0x42000000, v105
	v_mul_f32_e32 v109, 0x42000000, v109
	v_mul_f32_e32 v113, 0x42000000, v113
	v_mul_f32_e32 v117, 0x42000000, v117
	v_mul_f32_e32 v121, 0x42000000, v121
	v_mul_f32_e32 v125, 0x42000000, v125
	v_med3_f32 v65, v65, s28, v149
	v_med3_f32 v69, v69, s28, v149
	v_med3_f32 v73, v73, s28, v149
	v_med3_f32 v77, v77, s28, v149
	v_med3_f32 v81, v81, s28, v149
	v_med3_f32 v85, v85, s28, v149
	v_med3_f32 v89, v89, s28, v149
	v_med3_f32 v93, v93, s28, v149
	v_med3_f32 v97, v97, s28, v149
	v_med3_f32 v101, v101, s28, v149
	v_med3_f32 v105, v105, s28, v149
	v_med3_f32 v109, v109, s28, v149
	v_med3_f32 v113, v113, s28, v149
	v_med3_f32 v117, v117, s28, v149
	v_med3_f32 v121, v121, s28, v149
	v_med3_f32 v125, v125, s28, v149
	v_cvt_pk_fp8_f32 v140, v65, v69
	v_cvt_pk_fp8_f32 v141, v81, v85
	v_cvt_pk_fp8_f32 v142, v97, v101
	v_cvt_pk_fp8_f32 v143, v113, v117
	v_cvt_pk_fp8_f32 v140, v73, v77 op_sel:[0,0,1]
	v_cvt_pk_fp8_f32 v141, v89, v93 op_sel:[0,0,1]
	v_cvt_pk_fp8_f32 v142, v105, v109 op_sel:[0,0,1]
	v_cvt_pk_fp8_f32 v143, v121, v125 op_sel:[0,0,1]
	s_nop 0
	global_store_dwordx4 v148, v[140:143], s[20:21] offset:1024
	v_mul_f32_e32 v66, 0x42000000, v66
	v_mul_f32_e32 v70, 0x42000000, v70
	v_mul_f32_e32 v74, 0x42000000, v74
	v_mul_f32_e32 v78, 0x42000000, v78
	v_mul_f32_e32 v82, 0x42000000, v82
	v_mul_f32_e32 v86, 0x42000000, v86
	v_mul_f32_e32 v90, 0x42000000, v90
	v_mul_f32_e32 v94, 0x42000000, v94
	v_mul_f32_e32 v98, 0x42000000, v98
	v_mul_f32_e32 v102, 0x42000000, v102
	v_mul_f32_e32 v106, 0x42000000, v106
	v_mul_f32_e32 v110, 0x42000000, v110
	v_mul_f32_e32 v114, 0x42000000, v114
	v_mul_f32_e32 v118, 0x42000000, v118
	v_mul_f32_e32 v122, 0x42000000, v122
	v_mul_f32_e32 v126, 0x42000000, v126
	v_med3_f32 v66, v66, s28, v149
	v_med3_f32 v70, v70, s28, v149
	v_med3_f32 v74, v74, s28, v149
	v_med3_f32 v78, v78, s28, v149
	v_med3_f32 v82, v82, s28, v149
	v_med3_f32 v86, v86, s28, v149
	v_med3_f32 v90, v90, s28, v149
	v_med3_f32 v94, v94, s28, v149
	v_med3_f32 v98, v98, s28, v149
	v_med3_f32 v102, v102, s28, v149
	v_med3_f32 v106, v106, s28, v149
	v_med3_f32 v110, v110, s28, v149
	v_med3_f32 v114, v114, s28, v149
	v_med3_f32 v118, v118, s28, v149
	v_med3_f32 v122, v122, s28, v149
	v_med3_f32 v126, v126, s28, v149
	v_cvt_pk_fp8_f32 v136, v66, v70
	v_cvt_pk_fp8_f32 v137, v82, v86
	v_cvt_pk_fp8_f32 v138, v98, v102
	v_cvt_pk_fp8_f32 v139, v114, v118
	v_cvt_pk_fp8_f32 v136, v74, v78 op_sel:[0,0,1]
	v_cvt_pk_fp8_f32 v137, v90, v94 op_sel:[0,0,1]
	v_cvt_pk_fp8_f32 v138, v106, v110 op_sel:[0,0,1]
	v_cvt_pk_fp8_f32 v139, v122, v126 op_sel:[0,0,1]
	s_nop 0
	global_store_dwordx4 v148, v[136:139], s[20:21] offset:2048
	v_mul_f32_e32 v67, 0x42000000, v67
	v_mul_f32_e32 v71, 0x42000000, v71
	v_mul_f32_e32 v75, 0x42000000, v75
	v_mul_f32_e32 v79, 0x42000000, v79
	v_mul_f32_e32 v83, 0x42000000, v83
	v_mul_f32_e32 v87, 0x42000000, v87
	v_mul_f32_e32 v91, 0x42000000, v91
	v_mul_f32_e32 v95, 0x42000000, v95
	v_mul_f32_e32 v99, 0x42000000, v99
	v_mul_f32_e32 v103, 0x42000000, v103
	v_mul_f32_e32 v107, 0x42000000, v107
	v_mul_f32_e32 v111, 0x42000000, v111
	v_mul_f32_e32 v115, 0x42000000, v115
	v_mul_f32_e32 v119, 0x42000000, v119
	v_mul_f32_e32 v123, 0x42000000, v123
	v_mul_f32_e32 v127, 0x42000000, v127
	v_med3_f32 v67, v67, s28, v149
	v_med3_f32 v71, v71, s28, v149
	v_med3_f32 v75, v75, s28, v149
	v_med3_f32 v79, v79, s28, v149
	v_med3_f32 v83, v83, s28, v149
	v_med3_f32 v87, v87, s28, v149
	v_med3_f32 v91, v91, s28, v149
	v_med3_f32 v95, v95, s28, v149
	v_med3_f32 v99, v99, s28, v149
	v_med3_f32 v103, v103, s28, v149
	v_med3_f32 v107, v107, s28, v149
	v_med3_f32 v111, v111, s28, v149
	v_med3_f32 v115, v115, s28, v149
	v_med3_f32 v119, v119, s28, v149
	v_med3_f32 v123, v123, s28, v149
	v_med3_f32 v127, v127, s28, v149
	v_cvt_pk_fp8_f32 v140, v67, v71
	v_cvt_pk_fp8_f32 v141, v83, v87
	v_cvt_pk_fp8_f32 v142, v99, v103
	v_cvt_pk_fp8_f32 v143, v115, v119
	v_cvt_pk_fp8_f32 v140, v75, v79 op_sel:[0,0,1]
	v_cvt_pk_fp8_f32 v141, v91, v95 op_sel:[0,0,1]
	v_cvt_pk_fp8_f32 v142, v107, v111 op_sel:[0,0,1]
	v_cvt_pk_fp8_f32 v143, v123, v127 op_sel:[0,0,1]
	s_nop 0
	global_store_dwordx4 v148, v[140:143], s[20:21] offset:3072
	s_cmp_ge_u32 s7, s6
	s_cbranch_scc1 .Lp1c0_done
	s_mov_b32 s4, s7
	s_add_i32 s7, s4, s5
	s_cmp_lt_u32 s7, s6
	s_cbranch_scc0 .Lp1c0_A_last
	s_lshr_b32 s22, s7, 8
	s_and_b32 s23, s7, 0xff
	s_and_b32 s27, s22, 1
	s_lshr_b32 s22, s22, 1
	s_cmp_eq_u32 s27, 0
	s_cselect_b64 s[16:17], s[12:13], s[14:15]
	s_add_i32 s22, s22, 37
	s_lshl_b32 s24, s22, 22
	s_lshr_b32 s25, s23, 5
	s_lshl_b32 s25, s25, 19
	s_and_b32 s26, s23, 31
	s_lshl_b32 s26, s26, 7
	s_add_i32 s24, s24, s25
	s_add_i32 s24, s24, s26
	s_add_u32 s16, s16, s24
	s_addc_u32 s17, s17, 0
	s_nop 0
	global_load_dwordx4 v[64:67], v144, s[16:17] nt
	global_load_dwordx4 v[68:71], v145, s[16:17] nt
	global_load_dwordx4 v[72:75], v146, s[16:17] nt
	global_load_dwordx4 v[76:79], v147, s[16:17] nt
	s_add_u32 s16, s16, 0x4000
	s_addc_u32 s17, s17, 0
	s_nop 0
	global_load_dwordx4 v[80:83], v144, s[16:17] nt
	global_load_dwordx4 v[84:87], v145, s[16:17] nt
	global_load_dwordx4 v[88:91], v146, s[16:17] nt
	global_load_dwordx4 v[92:95], v147, s[16:17] nt
	s_add_u32 s16, s16, 0x4000
	s_addc_u32 s17, s17, 0
	s_nop 0
	global_load_dwordx4 v[96:99], v144, s[16:17] nt
	global_load_dwordx4 v[100:103], v145, s[16:17] nt
	global_load_dwordx4 v[104:107], v146, s[16:17] nt
	global_load_dwordx4 v[108:111], v147, s[16:17] nt
	s_add_u32 s16, s16, 0x4000
	s_addc_u32 s17, s17, 0
	s_nop 0
	global_load_dwordx4 v[112:115], v144, s[16:17] nt
	global_load_dwordx4 v[116:119], v145, s[16:17] nt
	global_load_dwordx4 v[120:123], v146, s[16:17] nt
	global_load_dwordx4 v[124:127], v147, s[16:17] nt
	s_waitcnt vmcnt(20)
	s_branch .Lp1c0_A_st

.Lp1c0_A_st:
	s_lshr_b32 s22, s4, 8
	s_and_b32 s23, s4, 0xff
	s_and_b32 s27, s22, 1
	s_lshr_b32 s22, s22, 1
	s_add_i32 s22, s22, 37
	s_mul_i32 s24, s22, 0x300000
	s_lshr_b32 s25, s23, 5
	s_lshl_b32 s25, s25, 7
	s_add_i32 s24, s24, s25
	s_and_b32 s26, s23, 31
	s_lshr_b32 s25, s26, 2
	s_lshl_b32 s25, s25, 18
	s_add_i32 s24, s24, s25
	s_lshl_b32 s25, s27, 17
	s_add_i32 s24, s24, s25
	s_and_b32 s25, s26, 3
	s_lshl_b32 s25, s25, 15
	s_add_i32 s24, s24, s25
	s_add_u32 s20, s10, s24
	s_addc_u32 s21, s11, 0
	v_mul_f32_e32 v0, 0x42000000, v0
	v_mul_f32_e32 v4, 0x42000000, v4
	v_mul_f32_e32 v8, 0x42000000, v8
	v_mul_f32_e32 v12, 0x42000000, v12
	v_mul_f32_e32 v16, 0x42000000, v16
	v_mul_f32_e32 v20, 0x42000000, v20
	v_mul_f32_e32 v24, 0x42000000, v24
	v_mul_f32_e32 v28, 0x42000000, v28
	v_mul_f32_e32 v32, 0x42000000, v32
	v_mul_f32_e32 v36, 0x42000000, v36
	v_mul_f32_e32 v40, 0x42000000, v40
	v_mul_f32_e32 v44, 0x42000000, v44
	v_mul_f32_e32 v48, 0x42000000, v48
	v_mul_f32_e32 v52, 0x42000000, v52
	v_mul_f32_e32 v56, 0x42000000, v56
	v_mul_f32_e32 v60, 0x42000000, v60
	v_med3_f32 v0, v0, s28, v149
	v_med3_f32 v4, v4, s28, v149
	v_med3_f32 v8, v8, s28, v149
	v_med3_f32 v12, v12, s28, v149
	v_med3_f32 v16, v16, s28, v149
	v_med3_f32 v20, v20, s28, v149
	v_med3_f32 v24, v24, s28, v149
	v_med3_f32 v28, v28, s28, v149
	v_med3_f32 v32, v32, s28, v149
	v_med3_f32 v36, v36, s28, v149
	v_med3_f32 v40, v40, s28, v149
	v_med3_f32 v44, v44, s28, v149
	v_med3_f32 v48, v48, s28, v149
	v_med3_f32 v52, v52, s28, v149
	v_med3_f32 v56, v56, s28, v149
	v_med3_f32 v60, v60, s28, v149
	v_cvt_pk_fp8_f32 v136, v0, v4
	v_cvt_pk_fp8_f32 v137, v16, v20
	v_cvt_pk_fp8_f32 v138, v32, v36
	v_cvt_pk_fp8_f32 v139, v48, v52
	v_cvt_pk_fp8_f32 v136, v8, v12 op_sel:[0,0,1]
	v_cvt_pk_fp8_f32 v137, v24, v28 op_sel:[0,0,1]
	v_cvt_pk_fp8_f32 v138, v40, v44 op_sel:[0,0,1]
	v_cvt_pk_fp8_f32 v139, v56, v60 op_sel:[0,0,1]
	s_nop 0
	global_store_dwordx4 v148, v[136:139], s[20:21]
	v_mul_f32_e32 v1, 0x42000000, v1
	v_mul_f32_e32 v5, 0x42000000, v5
	v_mul_f32_e32 v9, 0x42000000, v9
	v_mul_f32_e32 v13, 0x42000000, v13
	v_mul_f32_e32 v17, 0x42000000, v17
	v_mul_f32_e32 v21, 0x42000000, v21
	v_mul_f32_e32 v25, 0x42000000, v25
	v_mul_f32_e32 v29, 0x42000000, v29
	v_mul_f32_e32 v33, 0x42000000, v33
	v_mul_f32_e32 v37, 0x42000000, v37
	v_mul_f32_e32 v41, 0x42000000, v41
	v_mul_f32_e32 v45, 0x42000000, v45
	v_mul_f32_e32 v49, 0x42000000, v49
	v_mul_f32_e32 v53, 0x42000000, v53
	v_mul_f32_e32 v57, 0x42000000, v57
	v_mul_f32_e32 v61, 0x42000000, v61
	v_med3_f32 v1, v1, s28, v149
	v_med3_f32 v5, v5, s28, v149
	v_med3_f32 v9, v9, s28, v149
	v_med3_f32 v13, v13, s28, v149
	v_med3_f32 v17, v17, s28, v149
	v_med3_f32 v21, v21, s28, v149
	v_med3_f32 v25, v25, s28, v149
	v_med3_f32 v29, v29, s28, v149
	v_med3_f32 v33, v33, s28, v149
	v_med3_f32 v37, v37, s28, v149
	v_med3_f32 v41, v41, s28, v149
	v_med3_f32 v45, v45, s28, v149
	v_med3_f32 v49, v49, s28, v149
	v_med3_f32 v53, v53, s28, v149
	v_med3_f32 v57, v57, s28, v149
	v_med3_f32 v61, v61, s28, v149
	v_cvt_pk_fp8_f32 v140, v1, v5
	v_cvt_pk_fp8_f32 v141, v17, v21
	v_cvt_pk_fp8_f32 v142, v33, v37
	v_cvt_pk_fp8_f32 v143, v49, v53
	v_cvt_pk_fp8_f32 v140, v9, v13 op_sel:[0,0,1]
	v_cvt_pk_fp8_f32 v141, v25, v29 op_sel:[0,0,1]
	v_cvt_pk_fp8_f32 v142, v41, v45 op_sel:[0,0,1]
	v_cvt_pk_fp8_f32 v143, v57, v61 op_sel:[0,0,1]
	s_nop 0
	global_store_dwordx4 v148, v[140:143], s[20:21] offset:1024
	v_mul_f32_e32 v2, 0x42000000, v2
	v_mul_f32_e32 v6, 0x42000000, v6
	v_mul_f32_e32 v10, 0x42000000, v10
	v_mul_f32_e32 v14, 0x42000000, v14
	v_mul_f32_e32 v18, 0x42000000, v18
	v_mul_f32_e32 v22, 0x42000000, v22
	v_mul_f32_e32 v26, 0x42000000, v26
	v_mul_f32_e32 v30, 0x42000000, v30
	v_mul_f32_e32 v34, 0x42000000, v34
	v_mul_f32_e32 v38, 0x42000000, v38
	v_mul_f32_e32 v42, 0x42000000, v42
	v_mul_f32_e32 v46, 0x42000000, v46
	v_mul_f32_e32 v50, 0x42000000, v50
	v_mul_f32_e32 v54, 0x42000000, v54
	v_mul_f32_e32 v58, 0x42000000, v58
	v_mul_f32_e32 v62, 0x42000000, v62
	v_med3_f32 v2, v2, s28, v149
	v_med3_f32 v6, v6, s28, v149
	v_med3_f32 v10, v10, s28, v149
	v_med3_f32 v14, v14, s28, v149
	v_med3_f32 v18, v18, s28, v149
	v_med3_f32 v22, v22, s28, v149
	v_med3_f32 v26, v26, s28, v149
	v_med3_f32 v30, v30, s28, v149
	v_med3_f32 v34, v34, s28, v149
	v_med3_f32 v38, v38, s28, v149
	v_med3_f32 v42, v42, s28, v149
	v_med3_f32 v46, v46, s28, v149
	v_med3_f32 v50, v50, s28, v149
	v_med3_f32 v54, v54, s28, v149
	v_med3_f32 v58, v58, s28, v149
	v_med3_f32 v62, v62, s28, v149
	v_cvt_pk_fp8_f32 v136, v2, v6
	v_cvt_pk_fp8_f32 v137, v18, v22
	v_cvt_pk_fp8_f32 v138, v34, v38
	v_cvt_pk_fp8_f32 v139, v50, v54
	v_cvt_pk_fp8_f32 v136, v10, v14 op_sel:[0,0,1]
	v_cvt_pk_fp8_f32 v137, v26, v30 op_sel:[0,0,1]
	v_cvt_pk_fp8_f32 v138, v42, v46 op_sel:[0,0,1]
	v_cvt_pk_fp8_f32 v139, v58, v62 op_sel:[0,0,1]
	s_nop 0
	global_store_dwordx4 v148, v[136:139], s[20:21] offset:2048
	v_mul_f32_e32 v3, 0x42000000, v3
	v_mul_f32_e32 v7, 0x42000000, v7
	v_mul_f32_e32 v11, 0x42000000, v11
	v_mul_f32_e32 v15, 0x42000000, v15
	v_mul_f32_e32 v19, 0x42000000, v19
	v_mul_f32_e32 v23, 0x42000000, v23
	v_mul_f32_e32 v27, 0x42000000, v27
	v_mul_f32_e32 v31, 0x42000000, v31
	v_mul_f32_e32 v35, 0x42000000, v35
	v_mul_f32_e32 v39, 0x42000000, v39
	v_mul_f32_e32 v43, 0x42000000, v43
	v_mul_f32_e32 v47, 0x42000000, v47
	v_mul_f32_e32 v51, 0x42000000, v51
	v_mul_f32_e32 v55, 0x42000000, v55
	v_mul_f32_e32 v59, 0x42000000, v59
	v_mul_f32_e32 v63, 0x42000000, v63
	v_med3_f32 v3, v3, s28, v149
	v_med3_f32 v7, v7, s28, v149
	v_med3_f32 v11, v11, s28, v149
	v_med3_f32 v15, v15, s28, v149
	v_med3_f32 v19, v19, s28, v149
	v_med3_f32 v23, v23, s28, v149
	v_med3_f32 v27, v27, s28, v149
	v_med3_f32 v31, v31, s28, v149
	v_med3_f32 v35, v35, s28, v149
	v_med3_f32 v39, v39, s28, v149
	v_med3_f32 v43, v43, s28, v149
	v_med3_f32 v47, v47, s28, v149
	v_med3_f32 v51, v51, s28, v149
	v_med3_f32 v55, v55, s28, v149
	v_med3_f32 v59, v59, s28, v149
	v_med3_f32 v63, v63, s28, v149
	v_cvt_pk_fp8_f32 v140, v3, v7
	v_cvt_pk_fp8_f32 v141, v19, v23
	v_cvt_pk_fp8_f32 v142, v35, v39
	v_cvt_pk_fp8_f32 v143, v51, v55
	v_cvt_pk_fp8_f32 v140, v11, v15 op_sel:[0,0,1]
	v_cvt_pk_fp8_f32 v141, v27, v31 op_sel:[0,0,1]
	v_cvt_pk_fp8_f32 v142, v43, v47 op_sel:[0,0,1]
	v_cvt_pk_fp8_f32 v143, v59, v63 op_sel:[0,0,1]
	s_nop 0
	global_store_dwordx4 v148, v[140:143], s[20:21] offset:3072
	s_cmp_ge_u32 s7, s6
	s_cbranch_scc1 .Lp1c0_done
	s_mov_b32 s4, s7
	s_branch .Lp1c0_loop
.Lp1c0_done:
	s_mov_b64 s[10:11], s[8:9]
	s_add_u32 s0, s8, 0x148
	v_mbcnt_lo_u32_b32 v90, -1, 0
	v_mbcnt_hi_u32_b32 v90, -1, v90
	s_addc_u32 s1, s9, 0
	s_load_dword s16, s[8:9], 0x148
	v_readlane_b32 s2, v243, 0
	s_load_dwordx2 s[8:9], s[10:11], 0x130
	s_lshl_b32 s2, s2, 3
	s_add_i32 s14, s94, s2
	v_lshl_add_u32 v0, s14, 6, v90
	s_mov_b32 s2, 0x8800
	v_readlane_b32 s3, v243, 1
	v_cmp_gt_i32_e32 vcc, s2, v0
	s_and_saveexec_b64 s[2:3], vcc
	s_cbranch_execz .LBB0_188
	s_waitcnt lgkmcnt(0)
	s_add_u32 s4, s8, 0x34800000
	s_load_dwordx2 s[6:7], s[10:11], 0x38
	s_addc_u32 s5, s9, 0
	s_add_u32 s20, s8, 0x104000
	s_addc_u32 s21, s9, 0
	s_lshl_b32 s15, s16, 9
	s_mov_b64 s[12:13], 0
	s_mov_b32 s17, 0x78787879
	s_movk_i32 s18, 0x6000
	v_mov_b64_e32 v[2:3], s[20:21]
	s_mov_b32 s19, 0x87ff
